# instruction selection: canonicalizing self-maximum steps dropped from the NSA row maximum (on v14)
# speedup vs baseline: 1.0058x; 1.0058x over previous
.LBB0_2444:
	s_nop 0
	s_nop 0
	v_max_f32_e32 v98, v50, v51
	v_max3_f32 v99, v53, v54, v55
	v_max3_f32 v98, v98, v52, v56
	v_max3_f32 v99, v99, v58, v59
	v_max3_f32 v98, v98, v57, v60
	v_max3_f32 v99, v99, v62, v63
	v_max3_f32 v98, v98, v61, v64
	v_max3_f32 v98, v98, v65, v99
	v_mov_b32_e32 v99, v98
	s_nop 1
	v_permlane32_swap_b32_e32 v98, v99
	s_nop 0
	s_nop 0
	v_max_f32_e32 v98, v98, v99
	s_mov_b32 s84, 0x41000000
	v_cmp_lt_f32_e32 vcc, s84, v98
	s_cbranch_vccz .LBB0_2448
	s_nop 0
	v_max_f32_e32 v34, 0, v98
	v_exp_f32_e64 v142, -v34
	s_and_saveexec_b64 s[84:85], s[4:5]
	ds_write_b32 v183, v142 offset:57344
	s_or_b64 exec, exec, s[84:85]
	s_waitcnt lgkmcnt(0)
	v_add_u32_e32 v49, s75, v136
	ds_read_b128 v[144:147], v49 offset:57408
	ds_read_b128 v[148:151], v49 offset:57440
	ds_read_b128 v[152:155], v49 offset:57344
	ds_read_b128 v[204:207], v49 offset:57376
	s_waitcnt lgkmcnt(0)
	v_add_f32_e32 v140, v140, v34
	v_pk_add_f32 v[112:113], v[50:51], v[34:35] op_sel_hi:[1,0] neg_lo:[0,1] neg_hi:[0,1]
	v_pk_add_f32 v[110:111], v[52:53], v[34:35] op_sel_hi:[1,0] neg_lo:[0,1] neg_hi:[0,1]
	v_pk_add_f32 v[108:109], v[54:55], v[34:35] op_sel_hi:[1,0] neg_lo:[0,1] neg_hi:[0,1]
	v_pk_add_f32 v[106:107], v[56:57], v[34:35] op_sel_hi:[1,0] neg_lo:[0,1] neg_hi:[0,1]
	v_pk_add_f32 v[104:105], v[58:59], v[34:35] op_sel_hi:[1,0] neg_lo:[0,1] neg_hi:[0,1]
	v_pk_add_f32 v[102:103], v[60:61], v[34:35] op_sel_hi:[1,0] neg_lo:[0,1] neg_hi:[0,1]
	v_pk_add_f32 v[100:101], v[62:63], v[34:35] op_sel_hi:[1,0] neg_lo:[0,1] neg_hi:[0,1]
	v_pk_add_f32 v[98:99], v[64:65], v[34:35] op_sel_hi:[1,0] neg_lo:[0,1] neg_hi:[0,1]
	v_sub_f32_e32 v97, v97, v34
	v_sub_f32_e32 v96, v96, v34
	v_sub_f32_e32 v95, v95, v34
	v_sub_f32_e32 v94, v94, v34
	v_sub_f32_e32 v93, v93, v34
	v_sub_f32_e32 v92, v92, v34
	v_sub_f32_e32 v91, v91, v34
	v_sub_f32_e32 v90, v90, v34
	v_sub_f32_e32 v89, v89, v34
	v_sub_f32_e32 v88, v88, v34
	v_sub_f32_e32 v87, v87, v34
	v_sub_f32_e32 v86, v86, v34
	v_sub_f32_e32 v85, v85, v34
	v_sub_f32_e32 v84, v84, v34
	v_sub_f32_e32 v83, v83, v34
	v_sub_f32_e32 v82, v82, v34
	v_xor_b32_e32 v34, 0x80000000, v140
	v_mov_b32_e32 v35, v34
	v_mov_b32_e32 v36, v34
	v_mov_b32_e32 v37, v34
	v_mov_b32_e32 v38, v34
	v_mov_b32_e32 v39, v34
	v_mov_b32_e32 v40, v34
	v_mov_b32_e32 v41, v34
	v_mov_b32_e32 v42, v34
	v_mov_b32_e32 v43, v34
	v_mov_b32_e32 v44, v34
	v_mov_b32_e32 v45, v34
	v_mov_b32_e32 v46, v34
	v_mov_b32_e32 v47, v34
	v_mov_b32_e32 v48, v34
	v_mov_b32_e32 v49, v34
	v_mul_f32_e32 v202, v202, v142
	s_waitcnt lgkmcnt(2)
	v_pk_mul_f32 v[14:15], v[14:15], v[148:149]
	v_pk_mul_f32 v[10:11], v[10:11], v[144:145]
	s_waitcnt lgkmcnt(0)
	v_pk_mul_f32 v[6:7], v[6:7], v[204:205]
	v_pk_mul_f32 v[16:17], v[16:17], v[150:151]
	v_pk_mul_f32 v[12:13], v[12:13], v[146:147]
	v_pk_mul_f32 v[8:9], v[8:9], v[206:207]
	v_pk_mul_f32 v[4:5], v[4:5], v[154:155]
	v_pk_mul_f32 v[2:3], v[2:3], v[152:153]
	v_pk_mul_f32 v[30:31], v[30:31], v[148:149]
	v_pk_mul_f32 v[26:27], v[26:27], v[144:145]
	v_pk_mul_f32 v[22:23], v[22:23], v[204:205]
	v_pk_mul_f32 v[32:33], v[32:33], v[150:151]
	v_pk_mul_f32 v[28:29], v[28:29], v[146:147]
	v_pk_mul_f32 v[24:25], v[24:25], v[206:207]
	v_pk_mul_f32 v[20:21], v[20:21], v[154:155]
	v_pk_mul_f32 v[18:19], v[18:19], v[152:153]
	s_branch .LBB0_2449

.LBB0_2459:
	v_pk_add_f32 v[82:83], v[144:145], v[142:143]
	v_pk_add_f32 v[84:85], v[148:149], v[146:147]
	v_pk_add_f32 v[86:87], v[156:157], v[154:155]
	v_pk_add_f32 v[82:83], v[84:85], v[82:83]
	v_pk_add_f32 v[84:85], v[152:153], v[150:151]
	s_mov_b32 s72, 0x41000000
	v_pk_add_f32 v[84:85], v[86:87], v[84:85]
	s_nop 0
	v_pk_add_f32 v[82:83], v[84:85], v[82:83]
	s_nop 0
	v_add_f32_e32 v82, v82, v83
	s_nop 0
	v_max_f32_e32 v83, v98, v99
	v_max3_f32 v84, v101, v102, v103
	v_max3_f32 v83, v83, v100, v104
	v_max3_f32 v84, v84, v106, v107
	v_max3_f32 v83, v83, v105, v108
	v_max3_f32 v84, v84, v110, v111
	v_max3_f32 v83, v83, v109, v112
	v_max3_f32 v83, v83, v113, v84
	v_mov_b32_e32 v84, v83
	s_nop 1
	v_permlane32_swap_b32_e32 v83, v84
	s_nop 0
	s_nop 0
	v_max_f32_e32 v83, v83, v84
	v_add_f32_e32 v82, v202, v82
	v_cmp_lt_f32_e32 vcc, s72, v83
	s_cbranch_vccz .LBB0_2463
	s_nop 0
	v_max_f32_e32 v34, 0, v83
	v_exp_f32_e64 v83, -v34
	s_and_saveexec_b64 s[72:73], s[4:5]
	ds_write_b32 v183, v83 offset:57344
	s_or_b64 exec, exec, s[72:73]
	s_waitcnt lgkmcnt(0)
	v_add_u32_e32 v49, s75, v136
	ds_read_b128 v[84:87], v49 offset:57408
	ds_read_b128 v[88:91], v49 offset:57440
	ds_read_b128 v[92:95], v49 offset:57344
	ds_read_b128 v[142:145], v49 offset:57376
	s_waitcnt lgkmcnt(0)
	v_add_f32_e32 v140, v140, v34
	v_pk_add_f32 v[98:99], v[98:99], v[34:35] op_sel_hi:[1,0] neg_lo:[0,1] neg_hi:[0,1]
	v_pk_add_f32 v[100:101], v[100:101], v[34:35] op_sel_hi:[1,0] neg_lo:[0,1] neg_hi:[0,1]
	v_pk_add_f32 v[102:103], v[102:103], v[34:35] op_sel_hi:[1,0] neg_lo:[0,1] neg_hi:[0,1]
	v_pk_add_f32 v[104:105], v[104:105], v[34:35] op_sel_hi:[1,0] neg_lo:[0,1] neg_hi:[0,1]
	v_pk_add_f32 v[106:107], v[106:107], v[34:35] op_sel_hi:[1,0] neg_lo:[0,1] neg_hi:[0,1]
	v_pk_add_f32 v[108:109], v[108:109], v[34:35] op_sel_hi:[1,0] neg_lo:[0,1] neg_hi:[0,1]
	v_pk_add_f32 v[110:111], v[110:111], v[34:35] op_sel_hi:[1,0] neg_lo:[0,1] neg_hi:[0,1]
	v_pk_add_f32 v[112:113], v[112:113], v[34:35] op_sel_hi:[1,0] neg_lo:[0,1] neg_hi:[0,1]
	v_sub_f32_e32 v65, v65, v34
	v_sub_f32_e32 v64, v64, v34
	v_sub_f32_e32 v63, v63, v34
	v_sub_f32_e32 v62, v62, v34
	v_sub_f32_e32 v61, v61, v34
	v_sub_f32_e32 v60, v60, v34
	v_sub_f32_e32 v59, v59, v34
	v_sub_f32_e32 v58, v58, v34
	v_sub_f32_e32 v57, v57, v34
	v_sub_f32_e32 v56, v56, v34
	v_sub_f32_e32 v55, v55, v34
	v_sub_f32_e32 v54, v54, v34
	v_sub_f32_e32 v53, v53, v34
	v_sub_f32_e32 v52, v52, v34
	v_sub_f32_e32 v51, v51, v34
	v_sub_f32_e32 v50, v50, v34
	v_xor_b32_e32 v34, 0x80000000, v140
	v_mov_b32_e32 v35, v34
	v_mov_b32_e32 v36, v34
	v_mov_b32_e32 v37, v34
	v_mov_b32_e32 v38, v34
	v_mov_b32_e32 v39, v34
	v_mov_b32_e32 v40, v34
	v_mov_b32_e32 v41, v34
	v_mov_b32_e32 v42, v34
	v_mov_b32_e32 v43, v34
	v_mov_b32_e32 v44, v34
	v_mov_b32_e32 v45, v34
	v_mov_b32_e32 v46, v34
	v_mov_b32_e32 v47, v34
	v_mov_b32_e32 v48, v34
	v_mov_b32_e32 v49, v34
	v_mul_f32_e32 v82, v82, v83
	s_waitcnt lgkmcnt(2)
	v_pk_mul_f32 v[14:15], v[14:15], v[88:89]
	v_pk_mul_f32 v[10:11], v[10:11], v[84:85]
	s_waitcnt lgkmcnt(0)
	v_pk_mul_f32 v[6:7], v[6:7], v[142:143]
	v_pk_mul_f32 v[16:17], v[16:17], v[90:91]
	v_pk_mul_f32 v[12:13], v[12:13], v[86:87]
	v_pk_mul_f32 v[8:9], v[8:9], v[144:145]
	v_pk_mul_f32 v[4:5], v[4:5], v[94:95]
	v_pk_mul_f32 v[2:3], v[2:3], v[92:93]
	v_pk_mul_f32 v[30:31], v[30:31], v[88:89]
	v_pk_mul_f32 v[26:27], v[26:27], v[84:85]
	v_pk_mul_f32 v[22:23], v[22:23], v[142:143]
	v_pk_mul_f32 v[32:33], v[32:33], v[90:91]
	v_pk_mul_f32 v[28:29], v[28:29], v[86:87]
	v_pk_mul_f32 v[24:25], v[24:25], v[144:145]
	v_pk_mul_f32 v[20:21], v[20:21], v[94:95]
	v_pk_mul_f32 v[18:19], v[18:19], v[92:93]
